# P10: routing words (expert id, rank, gate) of the next row prefetched one iteration ahead
# speedup vs baseline: 1.0024x; 1.0024x over previous
.LBB0_1998:
	s_or_b64 exec, exec, s[4:5]
	s_cmpk_gt_i32 s72, 0x7fff
	s_waitcnt lgkmcnt(0)
	s_barrier
	s_cbranch_scc1 .LBB0_2001
	v_lshlrev_b32_e32 v16, 3, v32
	v_add_u32_e32 v8, 0x400, v16
	v_add_u32_e32 v0, 0x600, v16
	v_ashrrev_i32_e32 v17, 31, v16
	v_ashrrev_i32_e32 v9, 31, v8
	v_ashrrev_i32_e32 v1, 31, v0
	v_lshlrev_b64 v[44:45], 2, v[0:1]
	v_lshlrev_b64 v[46:47], 2, v[8:9]
	v_lshlrev_b64 v[48:49], 2, v[16:17]
	v_lshl_add_u64 v[10:11], s[28:29], 0, v[44:45]
	v_lshl_add_u64 v[18:19], s[28:29], 0, v[46:47]
	v_lshl_add_u64 v[34:35], s[28:29], 0, v[48:49]
	global_load_dwordx4 v[0:3], v[10:11], off offset:16
	global_load_dwordx4 v[4:7], v[10:11], off
	s_nop 0
	global_load_dwordx4 v[8:11], v[18:19], off offset:16
	global_load_dwordx4 v[12:15], v[18:19], off
	s_nop 0
	global_load_dwordx4 v[16:19], v[34:35], off offset:2064
	global_load_dwordx4 v[20:23], v[34:35], off offset:2048
	global_load_dwordx4 v[24:27], v[34:35], off offset:16
	global_load_dwordx4 v[28:31], v[34:35], off
	v_and_b32_e32 v34, 64, v33
	v_add_u32_e32 v34, 64, v34
	v_xor_b32_e32 v35, 1, v33
	v_cmp_lt_i32_e32 vcc, v35, v34
	s_ashr_i32 s73, s72, 31
	s_lshl_b64 s[0:1], s[72:73], 12
	v_cndmask_b32_e32 v35, v33, v35, vcc
	v_lshlrev_b32_e32 v157, 2, v35
	v_xor_b32_e32 v35, 2, v33
	v_cmp_lt_i32_e32 vcc, v35, v34
	s_ashr_i32 s75, s74, 31
	s_lshl_b64 s[2:3], s[72:73], 4
	v_cndmask_b32_e32 v35, v33, v35, vcc
	v_lshlrev_b32_e32 v196, 2, v35
	v_xor_b32_e32 v35, 4, v33
	v_cmp_lt_i32_e32 vcc, v35, v34
	s_lshl_b64 s[4:5], s[74:75], 4
	s_lshl_b64 s[6:7], s[72:73], 13
	v_cndmask_b32_e32 v35, v33, v35, vcc
	v_lshlrev_b32_e32 v197, 2, v35
	v_xor_b32_e32 v35, 8, v33
	v_cmp_lt_i32_e32 vcc, v35, v34
	v_mov_b32_e32 v201, 0x81400000
	v_mov_b32_e32 v202, 0x81200000
	v_cndmask_b32_e32 v35, v33, v35, vcc
	v_lshlrev_b32_e32 v198, 2, v35
	v_xor_b32_e32 v35, 16, v33
	v_cmp_lt_i32_e32 vcc, v35, v34
	s_mov_b32 s11, 0x71200000
	v_mov_b32_e32 v203, 0x81300000
	v_cndmask_b32_e32 v35, v33, v35, vcc
	v_lshlrev_b32_e32 v199, 2, v35
	v_xor_b32_e32 v35, 32, v33
	v_cmp_lt_i32_e32 vcc, v35, v34
	v_mov_b32_e32 v204, 0x3727c5ac
	s_mov_b32 s12, 0x800000
	v_cndmask_b32_e32 v33, v33, v35, vcc
	v_lshlrev_b32_e32 v200, 2, v33
	v_ashrrev_i32_e32 v33, 31, v32
	v_lshl_add_u64 v[52:53], v[32:33], 4, s[0:1]
	s_lshl_b64 s[0:1], s[74:75], 12
	s_add_u32 s6, s30, s6
	v_lshl_add_u64 v[50:51], v[32:33], 3, s[8:9]
	s_addc_u32 s7, s31, s7
	s_lshl_b64 s[8:9], s[74:75], 13
	s_add_i32 s10, 0, 0x20c00
	s_add_u32 s16, s34, s2
	s_addc_u32 s17, s35, s3
	global_load_dwordx4 v[224:227], v202, s[16:17]
	global_load_dwordx4 v[228:231], v203, s[16:17]
	global_load_dwordx4 v[236:239], v201, s[16:17]
	s_waitcnt vmcnt(0)
.LBB0_2000:
	s_add_u32 s14, s34, s2
	s_addc_u32 s15, s35, s3
	s_add_u32 s16, s14, s4
	s_addc_u32 s17, s15, s5
	s_waitcnt vmcnt(8)
	v_mov_b32_e32 v36, v224
	v_mov_b32_e32 v37, v225
	v_mov_b32_e32 v38, v226
	v_mov_b32_e32 v39, v227
	v_mov_b32_e32 v54, v228
	v_mov_b32_e32 v55, v229
	v_mov_b32_e32 v56, v230
	v_mov_b32_e32 v57, v231
	v_mov_b32_e32 v32, v236
	v_mov_b32_e32 v33, v237
	v_mov_b32_e32 v34, v238
	v_mov_b32_e32 v35, v239
	global_load_dwordx4 v[224:227], v202, s[16:17]
	global_load_dwordx4 v[228:231], v203, s[16:17]
	global_load_dwordx4 v[236:239], v201, s[16:17]
	v_lshl_add_u64 v[40:41], s[34:35], 0, v[52:53]
	v_add_co_u32_e32 v58, vcc, s11, v40
	v_lshlrev_b32_e32 v36, 2, v36
	v_addc_co_u32_e32 v59, vcc, 0, v41, vcc
	v_lshlrev_b32_e32 v37, 2, v37
	v_lshlrev_b32_e32 v38, 2, v38
	v_lshlrev_b32_e32 v39, 2, v39
	v_add_u32_e32 v36, s10, v36
	global_load_dwordx4 v[192:195], v[58:59], off
	global_load_dwordx4 v[206:209], v[58:59], off offset:1024
	v_add_u32_e32 v37, s10, v37
	v_add_u32_e32 v38, s10, v38
	v_add_u32_e32 v39, s10, v39
	ds_read_b32 v60, v36
	ds_read_b32 v61, v37
	ds_read_b32 v62, v38
	ds_read_b32 v63, v39
	global_load_dwordx4 v[40:43], v[58:59], off offset:2048
	global_load_dwordx4 v[36:39], v[58:59], off offset:3072
	s_waitcnt lgkmcnt(3)
	v_add_u32_e32 v54, v54, v60
	s_waitcnt lgkmcnt(2)
	v_add_u32_e32 v58, v55, v61
	s_waitcnt lgkmcnt(1)
	v_add_u32_e32 v56, v56, v62
	s_waitcnt lgkmcnt(0)
	v_add_u32_e32 v60, v57, v63
	v_ashrrev_i32_e32 v55, 31, v54
	v_ashrrev_i32_e32 v59, 31, v58
	v_ashrrev_i32_e32 v57, 31, v56
	v_ashrrev_i32_e32 v61, 31, v60
	v_lshlrev_b64 v[58:59], 11, v[58:59]
	v_lshlrev_b64 v[54:55], 11, v[54:55]
	v_lshlrev_b64 v[60:61], 11, v[60:61]
	v_lshlrev_b64 v[56:57], 11, v[56:57]
	v_lshl_add_u64 v[54:55], v[50:51], 0, v[54:55]
	v_lshl_add_u64 v[58:59], v[50:51], 0, v[58:59]
	v_lshl_add_u64 v[56:57], v[50:51], 0, v[56:57]
	v_lshl_add_u64 v[60:61], v[50:51], 0, v[60:61]
	global_load_dwordx2 v[62:63], v[54:55], off
	global_load_dwordx2 v[72:73], v[54:55], off offset:512
	global_load_dwordx2 v[104:105], v[54:55], off offset:1024
	global_load_dwordx2 v[136:137], v[54:55], off offset:1536
	global_load_dwordx2 v[64:65], v[58:59], off
	global_load_dwordx2 v[74:75], v[58:59], off offset:512
	global_load_dwordx2 v[106:107], v[58:59], off offset:1024
	global_load_dwordx2 v[138:139], v[58:59], off offset:1536
	global_load_dwordx2 v[70:71], v[56:57], off
	global_load_dwordx2 v[80:81], v[56:57], off offset:512
	global_load_dwordx2 v[112:113], v[56:57], off offset:1024
	global_load_dwordx2 v[144:145], v[56:57], off offset:1536
	global_load_dwordx2 v[82:83], v[60:61], off
	global_load_dwordx2 v[114:115], v[60:61], off offset:512
	global_load_dwordx2 v[146:147], v[60:61], off offset:1024
	global_load_dwordx2 v[58:59], v[60:61], off offset:1536
	s_waitcnt vmcnt(15)
	v_cvt_pk_f32_fp8_e32 v[92:93], v62
	v_cvt_pk_f32_fp8_sdwa v[94:95], v62 src0_sel:WORD_1
	v_cvt_pk_f32_fp8_e32 v[100:101], v63
	v_cvt_pk_f32_fp8_sdwa v[102:103], v63 src0_sel:WORD_1
	s_waitcnt vmcnt(11)
	v_cvt_pk_f32_fp8_e32 v[76:77], v64
	v_cvt_pk_f32_fp8_sdwa v[134:135], v73 src0_sel:WORD_1
	v_cvt_pk_f32_fp8_sdwa v[78:79], v64 src0_sel:WORD_1
	v_cvt_pk_f32_fp8_e32 v[84:85], v65
	v_cvt_pk_f32_fp8_sdwa v[86:87], v65 src0_sel:WORD_1
	s_waitcnt vmcnt(7)
	v_cvt_pk_f32_fp8_e32 v[64:65], v70
	v_cvt_pk_f32_fp8_e32 v[124:125], v72
	v_cvt_pk_f32_fp8_sdwa v[126:127], v72 src0_sel:WORD_1
	v_cvt_pk_f32_fp8_e32 v[132:133], v73
	v_cvt_pk_f32_fp8_sdwa v[118:119], v75 src0_sel:WORD_1
	v_cvt_pk_f32_fp8_e32 v[158:159], v104
	v_cvt_pk_f32_fp8_sdwa v[160:161], v104 src0_sel:WORD_1
	v_cvt_pk_f32_fp8_e32 v[166:167], v105
	v_cvt_pk_f32_fp8_sdwa v[168:169], v105 src0_sel:WORD_1
	v_cvt_pk_f32_fp8_e32 v[178:179], v136
	v_cvt_pk_f32_fp8_sdwa v[180:181], v136 src0_sel:WORD_1
	v_cvt_pk_f32_fp8_e32 v[182:183], v137
	v_cvt_pk_f32_fp8_sdwa v[184:185], v137 src0_sel:WORD_1
	v_cvt_pk_f32_fp8_sdwa v[66:67], v70 src0_sel:WORD_1
	v_cvt_pk_f32_fp8_e32 v[68:69], v71
	v_cvt_pk_f32_fp8_sdwa v[70:71], v71 src0_sel:WORD_1
	s_waitcnt vmcnt(3)
	v_cvt_pk_f32_fp8_e32 v[54:55], v82
	v_cvt_pk_f32_fp8_e32 v[108:109], v74
	v_cvt_pk_f32_fp8_sdwa v[110:111], v74 src0_sel:WORD_1
	v_cvt_pk_f32_fp8_e32 v[116:117], v75
	v_cvt_pk_f32_fp8_sdwa v[98:99], v81 src0_sel:WORD_1
	v_cvt_pk_f32_fp8_e32 v[140:141], v106
	v_cvt_pk_f32_fp8_sdwa v[142:143], v106 src0_sel:WORD_1
	v_cvt_pk_f32_fp8_e32 v[148:149], v107
	v_cvt_pk_f32_fp8_sdwa v[150:151], v107 src0_sel:WORD_1
	v_cvt_pk_f32_fp8_e32 v[170:171], v138
	v_cvt_pk_f32_fp8_sdwa v[172:173], v138 src0_sel:WORD_1
	v_cvt_pk_f32_fp8_e32 v[174:175], v139
	v_cvt_pk_f32_fp8_sdwa v[176:177], v139 src0_sel:WORD_1
	v_lshlrev_b32_e32 v190, 16, v192
	v_and_b32_e32 v191, 0xffff0000, v192
	v_cvt_pk_f32_fp8_sdwa v[56:57], v82 src0_sel:WORD_1
	v_cvt_pk_f32_fp8_e32 v[60:61], v83
	v_cvt_pk_f32_fp8_sdwa v[62:63], v83 src0_sel:WORD_1
	v_cvt_pk_f32_fp8_e32 v[88:89], v80
	v_cvt_pk_f32_fp8_sdwa v[90:91], v80 src0_sel:WORD_1
	v_cvt_pk_f32_fp8_e32 v[96:97], v81
	s_waitcnt vmcnt(2)
	v_cvt_pk_f32_fp8_sdwa v[82:83], v115 src0_sel:WORD_1
	v_cvt_pk_f32_fp8_e32 v[120:121], v112
	v_cvt_pk_f32_fp8_sdwa v[122:123], v112 src0_sel:WORD_1
	v_cvt_pk_f32_fp8_e32 v[128:129], v113
	v_cvt_pk_f32_fp8_sdwa v[130:131], v113 src0_sel:WORD_1
	v_cvt_pk_f32_fp8_e32 v[152:153], v144
	v_cvt_pk_f32_fp8_sdwa v[154:155], v144 src0_sel:WORD_1
	v_cvt_pk_f32_fp8_e32 v[162:163], v145
	v_cvt_pk_f32_fp8_sdwa v[164:165], v145 src0_sel:WORD_1
	v_lshlrev_b32_e32 v186, 16, v194
	v_and_b32_e32 v187, 0xffff0000, v194
	v_lshlrev_b32_e32 v188, 16, v195
	v_and_b32_e32 v189, 0xffff0000, v195
	v_lshlrev_b32_e32 v192, 16, v193
	v_and_b32_e32 v193, 0xffff0000, v193
	v_lshlrev_b32_e32 v194, 16, v208
	v_and_b32_e32 v195, 0xffff0000, v208
	v_lshlrev_b32_e32 v208, 16, v209
	v_and_b32_e32 v209, 0xffff0000, v209
	v_pk_fma_f32 v[92:93], v[32:33], v[92:93], v[190:191] op_sel_hi:[0,1,1]
	v_cvt_pk_f32_fp8_sdwa v[74:75], v114 src0_sel:WORD_1
	v_lshlrev_b32_e32 v210, 16, v206
	v_and_b32_e32 v211, 0xffff0000, v206
	v_lshlrev_b32_e32 v206, 16, v207
	v_and_b32_e32 v207, 0xffff0000, v207
	v_lshlrev_b32_e32 v212, 16, v42
	v_and_b32_e32 v213, 0xffff0000, v42
	v_lshlrev_b32_e32 v42, 16, v43
	v_and_b32_e32 v43, 0xffff0000, v43
	v_lshlrev_b32_e32 v214, 16, v40
	v_and_b32_e32 v215, 0xffff0000, v40
	v_lshlrev_b32_e32 v216, 16, v41
	v_and_b32_e32 v217, 0xffff0000, v41
	v_lshlrev_b32_e32 v218, 16, v38
	v_and_b32_e32 v219, 0xffff0000, v38
	v_lshlrev_b32_e32 v38, 16, v39
	v_and_b32_e32 v39, 0xffff0000, v39
	v_lshlrev_b32_e32 v220, 16, v36
	v_and_b32_e32 v221, 0xffff0000, v36
	v_lshlrev_b32_e32 v36, 16, v37
	v_and_b32_e32 v37, 0xffff0000, v37
	v_pk_fma_f32 v[100:101], v[32:33], v[100:101], v[186:187] op_sel_hi:[0,1,1]
	v_pk_fma_f32 v[102:103], v[32:33], v[102:103], v[188:189] op_sel_hi:[0,1,1]
	v_pk_fma_f32 v[94:95], v[32:33], v[94:95], v[192:193] op_sel_hi:[0,1,1]
	v_pk_fma_f32 v[134:135], v[32:33], v[134:135], v[208:209] op_sel_hi:[0,1,1]
	v_pk_fma_f32 v[76:77], v[32:33], v[76:77], v[92:93] op_sel:[1,0,0]
	v_mov_b32_e32 v156, v35
	v_pk_fma_f32 v[132:133], v[32:33], v[132:133], v[194:195] op_sel_hi:[0,1,1]
	v_pk_fma_f32 v[124:125], v[32:33], v[124:125], v[210:211] op_sel_hi:[0,1,1]
	v_pk_fma_f32 v[126:127], v[32:33], v[126:127], v[206:207] op_sel_hi:[0,1,1]
	v_pk_fma_f32 v[166:167], v[32:33], v[166:167], v[212:213] op_sel_hi:[0,1,1]
	v_pk_fma_f32 v[42:43], v[32:33], v[168:169], v[42:43] op_sel_hi:[0,1,1]
	v_pk_fma_f32 v[158:159], v[32:33], v[158:159], v[214:215] op_sel_hi:[0,1,1]
	v_pk_fma_f32 v[160:161], v[32:33], v[160:161], v[216:217] op_sel_hi:[0,1,1]
	v_pk_fma_f32 v[168:169], v[32:33], v[182:183], v[218:219] op_sel_hi:[0,1,1]
	v_pk_fma_f32 v[38:39], v[32:33], v[184:185], v[38:39] op_sel_hi:[0,1,1]
	v_pk_fma_f32 v[178:179], v[32:33], v[178:179], v[220:221] op_sel_hi:[0,1,1]
	v_pk_fma_f32 v[36:37], v[32:33], v[180:181], v[36:37] op_sel_hi:[0,1,1]
	v_pk_fma_f32 v[84:85], v[32:33], v[84:85], v[100:101] op_sel:[1,0,0]
	v_pk_fma_f32 v[86:87], v[32:33], v[86:87], v[102:103] op_sel:[1,0,0]
	v_pk_fma_f32 v[78:79], v[32:33], v[78:79], v[94:95] op_sel:[1,0,0]
	v_pk_fma_f32 v[94:95], v[32:33], v[118:119], v[134:135] op_sel:[1,0,0]
	v_pk_fma_f32 v[64:65], v[34:35], v[64:65], v[76:77] op_sel_hi:[0,1,1]
	v_cvt_pk_f32_fp8_e32 v[72:73], v114
	v_pk_fma_f32 v[92:93], v[32:33], v[116:117], v[132:133] op_sel:[1,0,0]
	v_pk_fma_f32 v[100:101], v[32:33], v[108:109], v[124:125] op_sel:[1,0,0]
	v_pk_fma_f32 v[102:103], v[32:33], v[110:111], v[126:127] op_sel:[1,0,0]
	v_pk_fma_f32 v[108:109], v[32:33], v[148:149], v[166:167] op_sel:[1,0,0]
	v_pk_fma_f32 v[42:43], v[32:33], v[150:151], v[42:43] op_sel:[1,0,0]
	v_pk_fma_f32 v[110:111], v[32:33], v[140:141], v[158:159] op_sel:[1,0,0]
	v_pk_fma_f32 v[116:117], v[32:33], v[142:143], v[160:161] op_sel:[1,0,0]
	v_pk_fma_f32 v[118:119], v[32:33], v[174:175], v[168:169] op_sel:[1,0,0]
	v_pk_fma_f32 v[38:39], v[32:33], v[176:177], v[38:39] op_sel:[1,0,0]
	v_pk_fma_f32 v[124:125], v[32:33], v[170:171], v[178:179] op_sel:[1,0,0]
	v_pk_fma_f32 v[32:33], v[32:33], v[172:173], v[36:37] op_sel:[1,0,0]
	v_pk_fma_f32 v[36:37], v[34:35], v[68:69], v[84:85] op_sel_hi:[0,1,1]
	v_pk_fma_f32 v[68:69], v[34:35], v[70:71], v[86:87] op_sel_hi:[0,1,1]
	v_pk_fma_f32 v[66:67], v[34:35], v[66:67], v[78:79] op_sel_hi:[0,1,1]
	v_pk_fma_f32 v[76:77], v[34:35], v[98:99], v[94:95] op_sel_hi:[0,1,1]
	v_pk_fma_f32 v[54:55], v[156:157], v[54:55], v[64:65] op_sel_hi:[0,1,1]
	v_pk_fma_f32 v[70:71], v[34:35], v[96:97], v[92:93] op_sel_hi:[0,1,1]
	v_pk_fma_f32 v[78:79], v[34:35], v[88:89], v[100:101] op_sel_hi:[0,1,1]
	v_pk_fma_f32 v[84:85], v[34:35], v[90:91], v[102:103] op_sel_hi:[0,1,1]
	v_pk_fma_f32 v[86:87], v[34:35], v[128:129], v[108:109] op_sel_hi:[0,1,1]
	v_pk_fma_f32 v[42:43], v[34:35], v[130:131], v[42:43] op_sel_hi:[0,1,1]
	v_pk_fma_f32 v[88:89], v[34:35], v[120:121], v[110:111] op_sel_hi:[0,1,1]
	v_pk_fma_f32 v[90:91], v[34:35], v[122:123], v[116:117] op_sel_hi:[0,1,1]
	v_pk_fma_f32 v[92:93], v[34:35], v[162:163], v[118:119] op_sel_hi:[0,1,1]
	v_pk_fma_f32 v[38:39], v[34:35], v[164:165], v[38:39] op_sel_hi:[0,1,1]
	v_pk_fma_f32 v[94:95], v[34:35], v[152:153], v[124:125] op_sel_hi:[0,1,1]
	v_pk_fma_f32 v[32:33], v[34:35], v[154:155], v[32:33] op_sel_hi:[0,1,1]
	v_pk_fma_f32 v[34:35], v[156:157], v[60:61], v[36:37] op_sel_hi:[0,1,1]
	v_pk_fma_f32 v[36:37], v[156:157], v[62:63], v[68:69] op_sel_hi:[0,1,1]
	v_pk_fma_f32 v[56:57], v[156:157], v[56:57], v[66:67] op_sel_hi:[0,1,1]
	v_pk_fma_f32 v[62:63], v[156:157], v[82:83], v[76:77] op_sel_hi:[0,1,1]
	v_pk_mul_f32 v[82:83], v[54:55], v[54:55]
	v_cvt_pk_f32_fp8_e32 v[80:81], v115
	v_pk_fma_f32 v[66:67], v[156:157], v[74:75], v[84:85] op_sel_hi:[0,1,1]
	v_pk_mul_f32 v[84:85], v[56:57], v[56:57]
	v_add_f32_e32 v82, v82, v83
	v_add_f32_e32 v82, v82, v84
	s_waitcnt vmcnt(1)
	v_cvt_pk_f32_fp8_sdwa v[106:107], v146 src0_sel:WORD_1
	v_pk_fma_f32 v[64:65], v[156:157], v[72:73], v[78:79] op_sel_hi:[0,1,1]
	v_pk_mul_f32 v[78:79], v[34:35], v[34:35]
	v_add_f32_e32 v82, v82, v85
	v_add_f32_e32 v78, v82, v78
	s_waitcnt vmcnt(0)
	v_cvt_pk_f32_fp8_e32 v[144:145], v59
	v_pk_fma_f32 v[60:61], v[156:157], v[80:81], v[70:71] op_sel_hi:[0,1,1]
	v_pk_mul_f32 v[80:81], v[36:37], v[36:37]
	v_add_f32_e32 v78, v78, v79
	v_add_f32_e32 v78, v78, v80
	v_cvt_pk_f32_fp8_e32 v[112:113], v147
	v_pk_fma_f32 v[72:73], v[156:157], v[106:107], v[90:91] op_sel_hi:[0,1,1]
	v_pk_mul_f32 v[90:91], v[64:65], v[64:65]
	v_add_f32_e32 v78, v78, v81
	v_add_f32_e32 v78, v78, v90
	v_cvt_pk_f32_fp8_e32 v[104:105], v146
	v_pk_fma_f32 v[74:75], v[156:157], v[144:145], v[92:93] op_sel_hi:[0,1,1]
	v_pk_mul_f32 v[92:93], v[66:67], v[66:67]
	v_add_f32_e32 v78, v78, v91
	v_add_f32_e32 v78, v78, v92
	v_pk_fma_f32 v[68:69], v[156:157], v[112:113], v[86:87] op_sel_hi:[0,1,1]
	v_pk_mul_f32 v[86:87], v[60:61], v[60:61]
	v_add_f32_e32 v78, v78, v93
	v_add_f32_e32 v78, v78, v86
	v_pk_fma_f32 v[70:71], v[156:157], v[104:105], v[88:89] op_sel_hi:[0,1,1]
	v_pk_mul_f32 v[88:89], v[62:63], v[62:63]
	v_add_f32_e32 v78, v78, v87
	v_add_f32_e32 v78, v78, v88
	v_cvt_pk_f32_fp8_e32 v[136:137], v58
	v_pk_mul_f32 v[98:99], v[70:71], v[70:71]
	v_add_f32_e32 v78, v78, v89
	v_cvt_pk_f32_fp8_sdwa v[114:115], v147 src0_sel:WORD_1
	v_add_f32_e32 v78, v78, v98
	v_pk_mul_f32 v[100:101], v[72:73], v[72:73]
	v_add_f32_e32 v78, v78, v99
	v_add_f32_e32 v78, v78, v100
	v_pk_fma_f32 v[76:77], v[156:157], v[136:137], v[94:95] op_sel_hi:[0,1,1]
	v_pk_mul_f32 v[94:95], v[68:69], v[68:69]
	v_add_f32_e32 v78, v78, v101
	v_cvt_pk_f32_fp8_sdwa v[138:139], v58 src0_sel:WORD_1
	v_pk_fma_f32 v[42:43], v[156:157], v[114:115], v[42:43] op_sel_hi:[0,1,1]
	v_add_f32_e32 v78, v78, v94
	v_pk_mul_f32 v[96:97], v[42:43], v[42:43]
	v_add_f32_e32 v78, v78, v95
	v_add_f32_e32 v78, v78, v96
	v_pk_mul_f32 v[106:107], v[76:77], v[76:77]
	v_add_f32_e32 v78, v78, v97
	v_cvt_pk_f32_fp8_sdwa v[146:147], v59 src0_sel:WORD_1
	v_pk_fma_f32 v[32:33], v[156:157], v[138:139], v[32:33] op_sel_hi:[0,1,1]
	v_add_f32_e32 v78, v78, v106
	v_pk_mul_f32 v[108:109], v[32:33], v[32:33]
	v_add_f32_e32 v78, v78, v107
	v_add_f32_e32 v78, v78, v108
	v_pk_mul_f32 v[102:103], v[74:75], v[74:75]
	v_add_f32_e32 v78, v78, v109
	v_pk_fma_f32 v[38:39], v[156:157], v[146:147], v[38:39] op_sel_hi:[0,1,1]
	v_add_f32_e32 v78, v78, v102
	v_pk_mul_f32 v[104:105], v[38:39], v[38:39]
	v_add_f32_e32 v78, v78, v103
	v_add_f32_e32 v78, v78, v104
	v_add_f32_e32 v78, v78, v105
	ds_bpermute_b32 v79, v157, v78
	s_add_i32 s72, s72, s74
	s_add_u32 s2, s2, s4
	s_addc_u32 s3, s3, s5
	v_lshl_add_u64 v[58:59], s[6:7], 0, v[48:49]
	s_waitcnt lgkmcnt(0)
	v_add_f32_e32 v78, v78, v79
	ds_bpermute_b32 v79, v196, v78
	v_lshl_add_u64 v[40:41], s[6:7], 0, v[46:47]
	v_lshl_add_u64 v[222:223], s[6:7], 0, v[44:45]
	s_add_u32 s6, s6, s8
	s_addc_u32 s7, s7, s9
	s_waitcnt lgkmcnt(0)
	v_add_f32_e32 v78, v78, v79
	ds_bpermute_b32 v79, v197, v78
	v_lshl_add_u64 v[52:53], v[52:53], 0, s[0:1]
	s_cmp_lt_i32 s72, 0x8000
	s_waitcnt lgkmcnt(0)
	v_add_f32_e32 v78, v78, v79
	ds_bpermute_b32 v79, v198, v78
	s_waitcnt lgkmcnt(0)
	v_add_f32_e32 v78, v78, v79
	ds_bpermute_b32 v79, v199, v78
	s_waitcnt lgkmcnt(0)
	v_add_f32_e32 v78, v78, v79
	ds_bpermute_b32 v79, v200, v78
	s_waitcnt lgkmcnt(0)
	v_add_f32_e32 v78, v78, v79
	v_fmamk_f32 v78, v78, 0x3a000000, v204
	v_mul_f32_e32 v79, 0x4b800000, v78
	v_cmp_gt_f32_e32 vcc, s12, v78
	s_nop 1
	v_cndmask_b32_e32 v78, v78, v79, vcc
	v_rsq_f32_e32 v78, v78
	s_nop 0
	v_mul_f32_e32 v79, 0x45800000, v78
	v_cndmask_b32_e32 v78, v78, v79, vcc
	v_pk_mul_f32 v[54:55], v[78:79], v[54:55] op_sel_hi:[0,1]
	v_pk_mul_f32 v[56:57], v[78:79], v[56:57] op_sel_hi:[0,1]
	v_pk_mul_f32 v[80:81], v[78:79], v[34:35] op_sel_hi:[0,1]
	v_pk_mul_f32 v[36:37], v[78:79], v[36:37] op_sel_hi:[0,1]
	v_pk_mul_f32 v[64:65], v[78:79], v[64:65] op_sel_hi:[0,1]
	v_pk_mul_f32 v[66:67], v[78:79], v[66:67] op_sel_hi:[0,1]
	v_pk_mul_f32 v[60:61], v[78:79], v[60:61] op_sel_hi:[0,1]
	v_pk_mul_f32 v[62:63], v[78:79], v[62:63] op_sel_hi:[0,1]
	v_pk_mul_f32 v[70:71], v[78:79], v[70:71] op_sel_hi:[0,1]
	v_pk_mul_f32 v[72:73], v[78:79], v[72:73] op_sel_hi:[0,1]
	v_pk_mul_f32 v[68:69], v[78:79], v[68:69] op_sel_hi:[0,1]
	v_pk_mul_f32 v[42:43], v[78:79], v[42:43] op_sel_hi:[0,1]
	v_pk_mul_f32 v[76:77], v[78:79], v[76:77] op_sel_hi:[0,1]
	v_pk_mul_f32 v[82:83], v[78:79], v[32:33] op_sel_hi:[0,1]
	v_pk_mul_f32 v[84:85], v[78:79], v[74:75] op_sel_hi:[0,1]
	v_pk_mul_f32 v[78:79], v[78:79], v[38:39] op_sel_hi:[0,1]
	v_pk_mul_f32 v[34:35], v[30:31], v[56:57]
	v_pk_mul_f32 v[32:33], v[28:29], v[54:55]
	v_pk_mul_f32 v[38:39], v[26:27], v[36:37]
	v_pk_mul_f32 v[36:37], v[24:25], v[80:81]
	v_pk_mul_f32 v[56:57], v[22:23], v[66:67]
	v_pk_mul_f32 v[54:55], v[20:21], v[64:65]
	v_pk_mul_f32 v[62:63], v[18:19], v[62:63]
	v_pk_mul_f32 v[60:61], v[16:17], v[60:61]
	v_pk_mul_f32 v[66:67], v[14:15], v[72:73]
	v_pk_mul_f32 v[64:65], v[12:13], v[70:71]
	v_pk_mul_f32 v[70:71], v[10:11], v[42:43]
	v_pk_mul_f32 v[68:69], v[8:9], v[68:69]
	v_pk_mul_f32 v[74:75], v[6:7], v[82:83]
	v_pk_mul_f32 v[72:73], v[4:5], v[76:77]
	v_pk_mul_f32 v[78:79], v[2:3], v[78:79]
	v_pk_mul_f32 v[76:77], v[0:1], v[84:85]
	global_store_dwordx4 v[58:59], v[32:35], off
	global_store_dwordx4 v[58:59], v[36:39], off offset:16
	global_store_dwordx4 v[58:59], v[54:57], off offset:2048
	global_store_dwordx4 v[58:59], v[60:63], off offset:2064
	global_store_dwordx4 v[40:41], v[64:67], off
	global_store_dwordx4 v[40:41], v[68:71], off offset:16
	global_store_dwordx4 v[222:223], v[72:75], off
	global_store_dwordx4 v[222:223], v[76:79], off offset:16
	s_cbranch_scc1 .LBB0_2000
